# MLA steady loops: waves 0-3 loop rotated so the back-edge and address updates sit before the per-tile barrier; DMA global addresses precomputed in QK MFMA gaps
# speedup vs baseline: 1.0129x; 1.0035x over previous
; #define ISSUE_K(t, sl) do { glds16(Kg + (long)(t) * (KSLOT / 2), (unsigned)__builtin_amdgcn_readfirstlane(kdst + (sl) * KSLOT)); \
;         if (k2) glds16(Kg + (long)(t) * (KSLOT / 2) + 4096, (unsigned)__builtin_amdgcn_readfirstlane(kdst + (sl) * KSLOT + 8192)); } while (0)
; #define ISSUE_V(t, sl) glds16(Vg + (long)(t) * 4096, (unsigned)__builtin_amdgcn_readfirstlane(vdst + (sl) * VSLOT))
; #define SFENCE() __builtin_amdgcn_sched_barrier(0)
; template <bool FOX>
; __device__ __forceinline__ void attn_unit(const Args& A, int b, int h, int qb, LAS char* shm, LAS float* dg) {
;     ...
;     const int t_end = (tw_last - t0 + 2 < nti) ? tw_last - t0 + 2 : nti;
; #pragma unroll 1
;     for (int t = 1; t < t_end; ++t) {
;         if (t == 1 && 4 < nti) ISSUE_K(t0 + 4, 0);
;         if (t + 4 < nti) ISSUE_K(t0 + t + 4, t % NS);
;         if (t + 2 < nti) ISSUE_V(t0 + t + 2, (t + 2) % NS);
;         SFENCE();
.LBB0_825:
	s_add_i32 s27, s26, 3
	s_cmp_lt_u32 s27, s94
	s_cbranch_scc0 .LBB0_828
	s_cmp_lg_u32 s98, 0
	s_cbranch_scc0 .Lmla_ss_no
	s_cmp_lg_u32 s26, s59
	s_cbranch_scc0 .Lmla_ss_no
	s_and_b32 s52, s27, 3
	s_mulk_i32 s52, 0x3000
	s_add_i32 s52, s52, s91
	s_add_i32 s53, s42, 0x6000
	s_and_b32 s53, s53, 0x6000
	s_add_i32 s53, s53, s93
	v_lshl_add_u64 v[250:251], v[232:233], 0, s[42:43]
	v_lshl_add_u64 v[240:241], v[234:235], 0, s[56:57]
	s_cmp_lt_i32 s89, 4
	s_cbranch_scc1 .Lmla_ss1_in
	s_branch .Lmla_ss2_top

; template <bool FOX>
; __device__ __forceinline__ void attn_unit(const Args& A, int b, int h, int qb, LAS char* shm, LAS float* dg) {
;     ...
;     for (int t = 1; t < t_end; ++t) {
;         if (t == 1 && 4 < nti) ISSUE_K(t0 + 4, 0);
;         if (t + 4 < nti) ISSUE_K(t0 + t + 4, t % NS);
;         if (t + 2 < nti) ISSUE_V(t0 + t + 2, (t + 2) % NS);
;         SFENCE();
;         { if constexpr (!FOX) { if (t0 + t == tw_last + 1) {
; #pragma unroll
;                   for (int r = 0; r < 16; ++r) negm[r] = -INFINITY;
;                   asm volatile("" : "+v"(negm)); } }
;           const lds_cptr vp = vp0 + ((t - 1) % NS) * VSLOT; float sa = 0.f, sb = 0.f;
; #pragma unroll
;           for (int g = 0; g < 2 * NQ; ++g) {
;               if (!FOX && g == 0) c0 = __builtin_amdgcn_mfma_f32_32x32x16_bf16(kf[0], qr[0], negm, 0, 0, 0);
;               else if (!FOX && g == 1) c1 = __builtin_amdgcn_mfma_f32_32x32x16_bf16(kf[1], qr[0], negm, 0, 0, 0);
;               else if (g & 1) c1 = __builtin_amdgcn_mfma_f32_32x32x16_bf16(kf[g], qr[g >> 1], c1, 0, 0, 0); else c0 = __builtin_amdgcn_mfma_f32_32x32x16_bf16(kf[g], qr[g >> 1], c0, 0, 0, 0);
;               if (g < 8) { const int i = (g >> 1) + 4 * (g & 1); vlo[i] = vtr(vp + (i >> 2) * 4096 + (i & 3) * 1024); vhi[i] = vtr(vp + (i >> 2) * 4096 + (i & 3) * 1024 + 512);
;                   if (g < 4) { sa += pp0[4 * g]; sb += pp0[4 * g + 1]; sa += pp0[4 * g + 2]; sb += pp0[4 * g + 3]; } else { sa += pp1[4 * g - 16]; sb += pp1[4 * g - 15]; sa += pp1[4 * g - 14]; sb += pp1[4 * g - 13]; }
;                   asm volatile("" : "+v"(sa), "+v"(sb)); }
;               { constexpr int G0 = FOX ? 0 : 4; if (g >= G0) { const int q = 2 * (g - G0);
; #pragma unroll
;                   for (int k = 0; k < 2; ++k) { const int w = q + k; const unsigned pkd = w < 8 ? cvt_pk_bf16(pp0[2 * w], pp0[2 * w + 1]) : cvt_pk_bf16(pp1[2 * w - 16], pp1[2 * w - 15]); pw[w >> 2][w & 3] = pkd; } } }
;               SFENCE();
;           }
;           lrun += sa + sb; }
;         MASKONLY(t);
;         float rm; ROWMAX(rm);
;         bool resc = false;
;         if (__any(rm > THR)) { const float dl = fmaxf(rm, 0.f); mhat += dl;
; #pragma unroll
;             for (int r = 0; r < 16; ++r) { c0[r] -= dl; c1[r] -= dl; }
;             if constexpr (!FOX) {
; #pragma unroll
;                 for (int r = 0; r < 16; ++r) negm[r] = -mhat;
.Lmla_ss1_top:
	s_waitcnt vmcnt(4)
	s_barrier
.Lmla_ss1_in:
	s_mov_b32 m0, s52
	s_nop 0
	global_load_lds_dwordx4 v[234:235], off
	s_add_i32 m0, s52, 0x2000
	s_nop 0
	global_load_lds_dwordx4 v[240:241], off
	s_mov_b32 m0, s53
	s_nop 0
	global_load_lds_dwordx4 v[250:251], off
	s_waitcnt lgkmcnt(0)
	s_add_i32 s27, s42, 0x8000
	v_mfma_f32_32x32x16_bf16 v[114:129], v[206:209], v[138:141], v[82:97]
	s_and_b32 s27, s27, 0x6000
	s_add_u32 s42, s42, 0x2000
	s_addc_u32 s43, s43, 0
	v_add_u32_e32 v3, s27, v247
	ds_read_b64_tr_b16 v[206:207], v3 offset:49152
	ds_read_b64_tr_b16 v[208:209], v3 offset:49664
	v_add_f32_e32 v4, 0, v67
	v_add_f32_e32 v5, 0, v66
	v_add_f32_e32 v4, v69, v4
	v_add_f32_e32 v5, v68, v5
	v_mfma_f32_32x32x16_bf16 v[98:113], v[194:197], v[138:141], v[82:97]
	ds_read_b64_tr_b16 v[194:195], v3 offset:53248
	ds_read_b64_tr_b16 v[196:197], v3 offset:53760
	v_add_f32_e32 v4, v71, v4
	v_add_f32_e32 v5, v70, v5
	v_add_f32_e32 v4, v73, v4
	v_add_f32_e32 v5, v72, v5
	v_mfma_f32_32x32x16_bf16 v[114:129], v[202:205], v[142:145], v[114:129]
	ds_read_b64_tr_b16 v[202:203], v3 offset:50176
	ds_read_b64_tr_b16 v[204:205], v3 offset:50688
	v_add_f32_e32 v4, v75, v4
	v_add_f32_e32 v5, v74, v5
	v_add_f32_e32 v4, v77, v4
	v_add_f32_e32 v5, v76, v5
	v_mfma_f32_32x32x16_bf16 v[98:113], v[186:189], v[142:145], v[98:113]
	ds_read_b64_tr_b16 v[214:215], v3 offset:54272
	ds_read_b64_tr_b16 v[216:217], v3 offset:54784
	v_add_f32_e32 v4, v79, v4
	v_add_f32_e32 v5, v78, v5
	v_add_f32_e32 v4, v81, v4
	v_add_f32_e32 v5, v80, v5
	v_mfma_f32_32x32x16_bf16 v[114:129], v[198:201], v[146:149], v[114:129]
	ds_read_b64_tr_b16 v[210:211], v3 offset:51200
	ds_read_b64_tr_b16 v[212:213], v3 offset:51712
	v_add_f32_e32 v4, v51, v4
	v_add_f32_e32 v5, v50, v5
	v_add_f32_e32 v4, v53, v4
	v_add_f32_e32 v5, v52, v5
	v_mfma_f32_32x32x16_bf16 v[98:113], v[182:185], v[146:149], v[98:113]
	ds_read_b64_tr_b16 v[12:13], v3 offset:55296
	ds_read_b64_tr_b16 v[14:15], v3 offset:55808
	v_add_f32_e32 v4, v55, v4
	v_add_f32_e32 v5, v54, v5
	v_add_f32_e32 v4, v57, v4
	v_add_f32_e32 v5, v56, v5
	v_mfma_f32_32x32x16_bf16 v[114:129], v[190:193], v[150:153], v[114:129]
	ds_read_b64_tr_b16 v[8:9], v3 offset:52224
	ds_read_b64_tr_b16 v[10:11], v3 offset:52736
	v_add_f32_e32 v4, v59, v4
	v_add_f32_e32 v16, v61, v4
	v_add_f32_e32 v4, v58, v5
	v_add_f32_e32 v17, v60, v4
	v_mfma_f32_32x32x16_bf16 v[98:113], v[170:173], v[150:153], v[98:113]
	v_lshl_add_u64 v[234:235], v[234:235], 0, s[62:63]
	s_and_b32 s64, s26, 3
	ds_read_b64_tr_b16 v[4:5], v3 offset:56320
	ds_read_b64_tr_b16 v[6:7], v3 offset:56832
	v_add_f32_e32 v3, v63, v16
	v_add_f32_e32 v16, v62, v17
	v_add_f32_e32 v3, v65, v3
	v_add_f32_e32 v16, v64, v16
	v_mfma_f32_32x32x16_bf16 v[114:129], v[178:181], v[154:157], v[114:129]
	s_mulk_i32 s64, 0x3000
	v_lshl_add_u64 v[250:251], v[232:233], 0, s[42:43]
	v_cvt_pk_bf16_f32 v178, v50, v51
	v_cvt_pk_bf16_f32 v179, v52, v53
	v_cvt_pk_bf16_f32 v186, v66, v67
	v_cvt_pk_bf16_f32 v187, v68, v69
	v_mfma_f32_32x32x16_bf16 v[98:113], v[166:169], v[154:157], v[98:113]
	s_add_i32 s52, s64, s91
	s_add_i32 s64, s42, 0x6000
	v_lshl_add_u64 v[240:241], v[234:235], 0, s[56:57]
	v_cvt_pk_bf16_f32 v180, v54, v55
	v_cvt_pk_bf16_f32 v181, v56, v57
	v_cvt_pk_bf16_f32 v188, v70, v71
	v_cvt_pk_bf16_f32 v189, v72, v73
	v_mfma_f32_32x32x16_bf16 v[114:129], v[174:177], v[158:161], v[114:129]
	s_and_b32 s64, s64, 0x6000
	s_add_i32 s53, s64, s93
	v_cvt_pk_bf16_f32 v218, v58, v59
	v_cvt_pk_bf16_f32 v219, v60, v61
	v_cvt_pk_bf16_f32 v182, v74, v75
	v_cvt_pk_bf16_f32 v183, v76, v77
	v_mfma_f32_32x32x16_bf16 v[98:113], v[162:165], v[158:161], v[98:113]
	v_cvt_pk_bf16_f32 v220, v62, v63
	v_cvt_pk_bf16_f32 v221, v64, v65
	v_cvt_pk_bf16_f32 v184, v78, v79
	v_cvt_pk_bf16_f32 v185, v80, v81
	v_add_f32_e32 v3, v3, v16
	v_add_f32_e32 v246, v246, v3
	s_nop 3
	s_waitcnt lgkmcnt(0)
	v_mfma_f32_32x32x16_bf16 v[18:33], v[186:189], v[206:209], v[18:33]
	s_add_i32 s27, s26, 1
	s_and_b32 s64, s27, 3
	s_mulk_i32 s64, 0x3000
	v_exp_f32_e32 v66, v114
	v_exp_f32_e32 v67, v115
	v_exp_f32_e32 v68, v116
	v_exp_f32_e32 v69, v117
	v_add_u32_e32 v3, s64, v248
	v_mfma_f32_32x32x16_bf16 v[34:49], v[186:189], v[194:197], v[34:49]
	v_exp_f32_e32 v70, v118
	v_exp_f32_e32 v71, v119
	v_exp_f32_e32 v72, v120
	v_exp_f32_e32 v73, v121
	ds_read_b128 v[206:209], v3
	ds_read_b128 v[194:197], v3 offset:512
	v_mfma_f32_32x32x16_bf16 v[18:33], v[182:185], v[202:205], v[18:33]
	v_exp_f32_e32 v74, v122
	v_exp_f32_e32 v75, v123
	v_exp_f32_e32 v76, v124
	v_exp_f32_e32 v77, v125
	ds_read_b128 v[202:205], v3 offset:2048
	ds_read_b128 v[186:189], v3 offset:2560
	v_mfma_f32_32x32x16_bf16 v[34:49], v[182:185], v[214:217], v[34:49]
	v_exp_f32_e32 v78, v126
	v_exp_f32_e32 v79, v127
	v_exp_f32_e32 v80, v128
	v_exp_f32_e32 v81, v129
	ds_read_b128 v[198:201], v3 offset:4096
	ds_read_b128 v[182:185], v3 offset:4608
	v_mfma_f32_32x32x16_bf16 v[18:33], v[178:181], v[210:213], v[18:33]
	v_exp_f32_e32 v50, v98
	v_exp_f32_e32 v51, v99
	v_exp_f32_e32 v52, v100
	v_exp_f32_e32 v53, v101
	ds_read_b128 v[190:193], v3 offset:6144
	ds_read_b128 v[170:173], v3 offset:6656
	v_mfma_f32_32x32x16_bf16 v[34:49], v[178:181], v[12:15], v[34:49]
	v_exp_f32_e32 v54, v102
	v_exp_f32_e32 v55, v103
	v_exp_f32_e32 v56, v104
	v_exp_f32_e32 v57, v105
	ds_read_b128 v[178:181], v3 offset:8192
	ds_read_b128 v[166:169], v3 offset:8704
	v_mfma_f32_32x32x16_bf16 v[18:33], v[218:221], v[8:11], v[18:33]
	v_exp_f32_e32 v58, v106
	v_exp_f32_e32 v59, v107
	v_exp_f32_e32 v60, v108
	v_exp_f32_e32 v61, v109
	ds_read_b128 v[174:177], v3 offset:10240
	ds_read_b128 v[162:165], v3 offset:10752
	v_mfma_f32_32x32x16_bf16 v[34:49], v[218:221], v[4:7], v[34:49]
	v_exp_f32_e32 v62, v110
	v_exp_f32_e32 v63, v111
	v_exp_f32_e32 v64, v112
	v_exp_f32_e32 v65, v113
	s_mov_b32 s26, s27
	s_cmp_eq_u32 s27, s96
	s_cbranch_scc1 .Lmla_ss1_xdone
	s_add_i32 s64, s27, 3
	s_cmp_lt_u32 s64, s94
	s_cbranch_scc1 .Lmla_ss1_top
	s_waitcnt vmcnt(4)
	s_barrier
	s_branch .Lmla_ss_back
; #define SFENCE() __builtin_amdgcn_sched_barrier(0)
; template <bool FOX>
; __device__ __forceinline__ void attn_unit(const Args& A, int b, int h, int qb, LAS char* shm, LAS float* dg) {
;     ...
;           const lds_cptr vp = vp0 + ((t - 1) % NS) * VSLOT; float sa = 0.f, sb = 0.f;
; #pragma unroll
;           for (int g = 0; g < 2 * NQ; ++g) {
;               if (!FOX && g == 0) c0 = __builtin_amdgcn_mfma_f32_32x32x16_bf16(kf[0], qr[0], negm, 0, 0, 0);
;               else if (!FOX && g == 1) c1 = __builtin_amdgcn_mfma_f32_32x32x16_bf16(kf[1], qr[0], negm, 0, 0, 0);
;               else if (g & 1) c1 = __builtin_amdgcn_mfma_f32_32x32x16_bf16(kf[g], qr[g >> 1], c1, 0, 0, 0); else c0 = __builtin_amdgcn_mfma_f32_32x32x16_bf16(kf[g], qr[g >> 1], c0, 0, 0, 0);
;               if (g < 8) { const int i = (g >> 1) + 4 * (g & 1); vlo[i] = vtr(vp + (i >> 2) * 4096 + (i & 3) * 1024); vhi[i] = vtr(vp + (i >> 2) * 4096 + (i & 3) * 1024 + 512);
;                   if (g < 4) { sa += pp0[4 * g]; sb += pp0[4 * g + 1]; sa += pp0[4 * g + 2]; sb += pp0[4 * g + 3]; } else { sa += pp1[4 * g - 16]; sb += pp1[4 * g - 15]; sa += pp1[4 * g - 14]; sb += pp1[4 * g - 13]; }
;                   asm volatile("" : "+v"(sa), "+v"(sb)); }
;               { constexpr int G0 = FOX ? 0 : 4; if (g >= G0) { const int q = 2 * (g - G0);
; #pragma unroll
;                   for (int k = 0; k < 2; ++k) { const int w = q + k; const unsigned pkd = w < 8 ? cvt_pk_bf16(pp0[2 * w], pp0[2 * w + 1]) : cvt_pk_bf16(pp1[2 * w - 16], pp1[2 * w - 15]); pw[w >> 2][w & 3] = pkd; } } }
;               SFENCE();
;           }
;           lrun += sa + sb; }
;         MASKONLY(t);
;         float rm; ROWMAX(rm);
;         bool resc = false;
;         if (__any(rm > THR)) { const float dl = fmaxf(rm, 0.f); mhat += dl;
; #pragma unroll
;             for (int r = 0; r < 16; ++r) { c0[r] -= dl; c1[r] -= dl; }
;             if constexpr (!FOX) {
; #pragma unroll
;                 for (int r = 0; r < 16; ++r) negm[r] = -mhat;
;                 asm volatile("" : "+v"(negm)); }
;             const float f = __builtin_amdgcn_exp2f(-dl); lrun *= f; if (hi == 0) wsf[r32] = f; resc = true; }
;         SFENCE();
;         { const lds_cptr kp = kp0 + ((t + 1) % NS) * KSLOT;
; #pragma unroll
;           for (int g = 0; g < 8; ++g) { const int i = (g >> 1) + 4 * (g & 1);
.Lmla_ss1_xdone:
	s_waitcnt vmcnt(4)
	s_barrier
	s_branch .Lmla_ss_done
.Lmla_ss2_top:
	s_mov_b32 m0, s52
	s_nop 0
	global_load_lds_dwordx4 v[234:235], off
	s_mov_b32 m0, s53
	s_nop 0
	global_load_lds_dwordx4 v[250:251], off
	s_waitcnt lgkmcnt(0)
	s_add_i32 s27, s42, 0x8000
	v_mfma_f32_32x32x16_bf16 v[114:129], v[206:209], v[138:141], v[82:97]
	s_and_b32 s27, s27, 0x6000
	s_add_u32 s42, s42, 0x2000
	s_addc_u32 s43, s43, 0
	v_add_u32_e32 v3, s27, v247
	ds_read_b64_tr_b16 v[206:207], v3 offset:49152
	ds_read_b64_tr_b16 v[208:209], v3 offset:49664
	v_add_f32_e32 v4, 0, v67
	v_add_f32_e32 v5, 0, v66
	v_add_f32_e32 v4, v69, v4
	v_add_f32_e32 v5, v68, v5
	v_mfma_f32_32x32x16_bf16 v[98:113], v[194:197], v[138:141], v[82:97]
	ds_read_b64_tr_b16 v[194:195], v3 offset:53248
	ds_read_b64_tr_b16 v[196:197], v3 offset:53760
	v_add_f32_e32 v4, v71, v4
	v_add_f32_e32 v5, v70, v5
	v_add_f32_e32 v4, v73, v4
	v_add_f32_e32 v5, v72, v5
	v_mfma_f32_32x32x16_bf16 v[114:129], v[202:205], v[142:145], v[114:129]
	ds_read_b64_tr_b16 v[202:203], v3 offset:50176
	ds_read_b64_tr_b16 v[204:205], v3 offset:50688
	v_add_f32_e32 v4, v75, v4
	v_add_f32_e32 v5, v74, v5
	v_add_f32_e32 v4, v77, v4
	v_add_f32_e32 v5, v76, v5
	v_mfma_f32_32x32x16_bf16 v[98:113], v[186:189], v[142:145], v[98:113]
	ds_read_b64_tr_b16 v[214:215], v3 offset:54272
	ds_read_b64_tr_b16 v[216:217], v3 offset:54784
	v_add_f32_e32 v4, v79, v4
	v_add_f32_e32 v5, v78, v5
	v_add_f32_e32 v4, v81, v4
	v_add_f32_e32 v5, v80, v5
	v_mfma_f32_32x32x16_bf16 v[114:129], v[198:201], v[146:149], v[114:129]
	ds_read_b64_tr_b16 v[210:211], v3 offset:51200
	ds_read_b64_tr_b16 v[212:213], v3 offset:51712
	v_add_f32_e32 v4, v51, v4
	v_add_f32_e32 v5, v50, v5
	v_add_f32_e32 v4, v53, v4
	v_add_f32_e32 v5, v52, v5
	v_mfma_f32_32x32x16_bf16 v[98:113], v[182:185], v[146:149], v[98:113]
	ds_read_b64_tr_b16 v[12:13], v3 offset:55296
	ds_read_b64_tr_b16 v[14:15], v3 offset:55808
	v_add_f32_e32 v4, v55, v4
	v_add_f32_e32 v5, v54, v5
	v_add_f32_e32 v4, v57, v4
	v_add_f32_e32 v5, v56, v5
	v_mfma_f32_32x32x16_bf16 v[114:129], v[190:193], v[150:153], v[114:129]
	ds_read_b64_tr_b16 v[8:9], v3 offset:52224
	ds_read_b64_tr_b16 v[10:11], v3 offset:52736
	v_add_f32_e32 v4, v59, v4
	v_add_f32_e32 v16, v61, v4
	v_add_f32_e32 v4, v58, v5
	v_add_f32_e32 v17, v60, v4
	v_mfma_f32_32x32x16_bf16 v[98:113], v[170:173], v[150:153], v[98:113]
	v_lshl_add_u64 v[234:235], v[234:235], 0, s[62:63]
	s_and_b32 s64, s26, 3
	ds_read_b64_tr_b16 v[4:5], v3 offset:56320
	ds_read_b64_tr_b16 v[6:7], v3 offset:56832
	v_add_f32_e32 v3, v63, v16
	v_add_f32_e32 v16, v62, v17
	v_add_f32_e32 v3, v65, v3
	v_add_f32_e32 v16, v64, v16
	v_mfma_f32_32x32x16_bf16 v[114:129], v[178:181], v[154:157], v[114:129]
	s_mulk_i32 s64, 0x3000
	v_lshl_add_u64 v[250:251], v[232:233], 0, s[42:43]
	v_cvt_pk_bf16_f32 v178, v50, v51
	v_cvt_pk_bf16_f32 v179, v52, v53
	v_cvt_pk_bf16_f32 v186, v66, v67
	v_cvt_pk_bf16_f32 v187, v68, v69
	v_mfma_f32_32x32x16_bf16 v[98:113], v[166:169], v[154:157], v[98:113]
	s_add_i32 s52, s64, s91
	s_add_i32 s64, s42, 0x6000
	v_cvt_pk_bf16_f32 v180, v54, v55
	v_cvt_pk_bf16_f32 v181, v56, v57
	v_cvt_pk_bf16_f32 v188, v70, v71
	v_cvt_pk_bf16_f32 v189, v72, v73
	v_mfma_f32_32x32x16_bf16 v[114:129], v[174:177], v[158:161], v[114:129]
	s_and_b32 s64, s64, 0x6000
	s_add_i32 s53, s64, s93
	v_cvt_pk_bf16_f32 v218, v58, v59
	v_cvt_pk_bf16_f32 v219, v60, v61
	v_cvt_pk_bf16_f32 v182, v74, v75
	v_cvt_pk_bf16_f32 v183, v76, v77
	v_mfma_f32_32x32x16_bf16 v[98:113], v[162:165], v[158:161], v[98:113]
	v_cvt_pk_bf16_f32 v220, v62, v63
	v_cvt_pk_bf16_f32 v221, v64, v65
	v_cvt_pk_bf16_f32 v184, v78, v79
	v_cvt_pk_bf16_f32 v185, v80, v81
	v_add_f32_e32 v3, v3, v16
	v_add_f32_e32 v246, v246, v3
	s_waitcnt vmcnt(3)
	s_waitcnt lgkmcnt(0)
	s_barrier
	v_mfma_f32_32x32x16_bf16 v[18:33], v[186:189], v[206:209], v[18:33]
	s_add_i32 s27, s26, 1
	s_and_b32 s64, s27, 3
	s_mulk_i32 s64, 0x3000
	v_exp_f32_e32 v66, v114
	v_exp_f32_e32 v67, v115
	v_exp_f32_e32 v68, v116
	v_exp_f32_e32 v69, v117
	v_add_u32_e32 v3, s64, v248
	v_mfma_f32_32x32x16_bf16 v[34:49], v[186:189], v[194:197], v[34:49]
	v_exp_f32_e32 v70, v118
	v_exp_f32_e32 v71, v119
	v_exp_f32_e32 v72, v120
	v_exp_f32_e32 v73, v121
	ds_read_b128 v[206:209], v3
	ds_read_b128 v[194:197], v3 offset:512
	v_mfma_f32_32x32x16_bf16 v[18:33], v[182:185], v[202:205], v[18:33]
	v_exp_f32_e32 v74, v122
	v_exp_f32_e32 v75, v123
	v_exp_f32_e32 v76, v124
	v_exp_f32_e32 v77, v125
	ds_read_b128 v[202:205], v3 offset:2048
	ds_read_b128 v[186:189], v3 offset:2560
	v_mfma_f32_32x32x16_bf16 v[34:49], v[182:185], v[214:217], v[34:49]
	v_exp_f32_e32 v78, v126
	v_exp_f32_e32 v79, v127
	v_exp_f32_e32 v80, v128
	v_exp_f32_e32 v81, v129
	ds_read_b128 v[198:201], v3 offset:4096
	ds_read_b128 v[182:185], v3 offset:4608
	v_mfma_f32_32x32x16_bf16 v[18:33], v[178:181], v[210:213], v[18:33]
	v_exp_f32_e32 v50, v98
	v_exp_f32_e32 v51, v99
	v_exp_f32_e32 v52, v100
	v_exp_f32_e32 v53, v101
	ds_read_b128 v[190:193], v3 offset:6144
	ds_read_b128 v[170:173], v3 offset:6656
	v_mfma_f32_32x32x16_bf16 v[34:49], v[178:181], v[12:15], v[34:49]
	v_exp_f32_e32 v54, v102
	v_exp_f32_e32 v55, v103
	v_exp_f32_e32 v56, v104
	v_exp_f32_e32 v57, v105
	ds_read_b128 v[178:181], v3 offset:8192
	ds_read_b128 v[166:169], v3 offset:8704
	v_mfma_f32_32x32x16_bf16 v[18:33], v[218:221], v[8:11], v[18:33]
	v_exp_f32_e32 v58, v106
	v_exp_f32_e32 v59, v107
	v_exp_f32_e32 v60, v108
	v_exp_f32_e32 v61, v109
	ds_read_b128 v[174:177], v3 offset:10240
	ds_read_b128 v[162:165], v3 offset:10752
	v_mfma_f32_32x32x16_bf16 v[34:49], v[218:221], v[4:7], v[34:49]
	v_exp_f32_e32 v62, v110
	v_exp_f32_e32 v63, v111
	v_exp_f32_e32 v64, v112
	v_exp_f32_e32 v65, v113
	s_mov_b32 s26, s27
	s_cmp_eq_u32 s27, s96
	s_cbranch_scc1 .Lmla_ss2_xdone
	s_add_i32 s64, s27, 3
	s_cmp_lt_u32 s64, s94
	s_cbranch_scc1 .Lmla_ss2_top
	s_branch .Lmla_ss_back
.Lmla_ss2_xdone:
	s_branch .Lmla_ss_done
.Lmla_ss_back:
	s_waitcnt lgkmcnt(0)
	s_mov_b64 s[60:61], 0
	s_branch .LBB0_825
